# full stack + static s_setprio 1 for waves 0-3 (older half) at the attention entry, reset at the next grid barrier
# speedup vs baseline: 1.0035x; 1.0035x over previous
.LBB0_942:
	s_cmpk_gt_i32 s56, 0x40f
	s_barrier
	s_cbranch_scc1 .LBB0_1085
	v_readfirstlane_b32 s32, v0
	s_nop 3
	s_bfe_u32 s32, s32, 0x40006
	s_cmp_ge_u32 s32, 4
	s_cbranch_scc1 .Laprio_L0
	s_setprio 1

.LBB0_2986:
	v_readlane_b32 s0, v254, 4
	v_readlane_b32 s1, v254, 5
	s_and_b64 vcc, exec, s[0:1]
	s_barrier
	s_cbranch_vccz .LBB0_3117
	v_readfirstlane_b32 s32, v0
	s_nop 3
	s_bfe_u32 s32, s32, 0x40006
	s_cmp_ge_u32 s32, 4
	s_cbranch_scc1 .Laprio_L1
	s_setprio 1
